# GEMM1 epilogue relu in the MP/node kernels: convert to f16 first, then relu with v_pk_max_f16 (8 cvt + 8 pk_max instead of 16 v_max_i32 + 8 cvt per wave-tile; round-then-relu equals relu-then-round)
# speedup vs baseline: 1.0029x; 1.0029x over previous
.LBB5_14:
	v_or_b32_e32 v0, s33, v200
	ds_read_b128 v[142:145], v0 offset:0
	s_waitcnt lgkmcnt(4)
	s_nop 0
	v_mfma_f32_16x16x32_f16 v[134:137], v[114:117], v[134:137], v[166:169]
	ds_read_b128 v[146:149], v0 offset:0x1000
	s_waitcnt lgkmcnt(4)
	s_nop 0
	v_mfma_f32_16x16x32_f16 v[138:141], v[114:117], v[138:141], v[170:173]
	ds_read_b128 v[150:153], v0 offset:0x2000
	s_waitcnt lgkmcnt(4)
	s_nop 0
	v_mfma_f32_16x16x32_f16 v[154:157], v[114:117], v[158:161], v[174:177]
	ds_read_b128 v[158:161], v0 offset:0x3000
	s_waitcnt lgkmcnt(4)
	s_nop 0
	v_mfma_f32_16x16x32_f16 v[162:165], v[114:117], v[162:165], v[178:181]
	ds_read_b128 v[166:169], v205 offset:0
	s_waitcnt lgkmcnt(4)
	s_nop 0
	v_mfma_f32_16x16x32_f16 v[134:137], v[106:109], v[142:145], v[134:137]
	ds_read_b128 v[142:145], v205 offset:0x100
	s_waitcnt lgkmcnt(4)
	s_nop 0
	v_mfma_f32_16x16x32_f16 v[138:141], v[106:109], v[146:149], v[138:141]
	ds_read_b128 v[146:149], v205 offset:0x200
	s_waitcnt lgkmcnt(4)
	s_nop 0
	v_mfma_f32_16x16x32_f16 v[150:153], v[106:109], v[150:153], v[154:157]
	ds_read_b128 v[154:157], v205 offset:0x300
	s_waitcnt lgkmcnt(4)
	s_nop 0
	v_mfma_f32_16x16x32_f16 v[158:161], v[106:109], v[158:161], v[162:165]
	s_waitcnt lgkmcnt(3)
	s_nop 0
	v_mfma_f32_16x16x32_f16 v[134:137], v[102:105], v[166:169], v[134:137]
	s_waitcnt lgkmcnt(2)
	s_nop 0
	v_mfma_f32_16x16x32_f16 v[138:141], v[102:105], v[142:145], v[138:141]
	s_waitcnt lgkmcnt(1)
	s_nop 0
	v_mfma_f32_16x16x32_f16 v[142:145], v[102:105], v[146:149], v[150:153]
	s_waitcnt lgkmcnt(0)
	s_nop 0
	v_mfma_f32_16x16x32_f16 v[146:149], v[102:105], v[154:157], v[158:161]
	s_nop 1
	v_cvt_pk_f16_f32 v1, v136, v137
	v_pk_max_f16 v1, v1, 0
	v_cvt_pk_f16_f32 v0, v134, v135
	v_pk_max_f16 v0, v0, 0
	v_cvt_pk_f16_f32 v135, v140, v141
	v_pk_max_f16 v135, v135, 0
	v_cvt_pk_f16_f32 v134, v138, v139
	v_pk_max_f16 v134, v134, 0
	ds_write2st64_b64 v218, v[0:1], v[134:135] offset1:8
	v_cvt_pk_f16_f32 v1, v144, v145
	v_pk_max_f16 v1, v1, 0
	v_cvt_pk_f16_f32 v0, v142, v143
	v_pk_max_f16 v0, v0, 0
	s_lshl_b32 s34, s2, 14
	v_cvt_pk_f16_f32 v135, v148, v149
	v_pk_max_f16 v135, v135, 0
	v_cvt_pk_f16_f32 v134, v146, v147
	v_pk_max_f16 v134, v134, 0
	s_or_b32 s34, s34, 0x18000
	ds_write2st64_b64 v218, v[0:1], v[134:135] offset0:16 offset1:24
	v_or_b32_e32 v172, s34, v197
	v_or_b32_e32 v223, s34, v198
	v_or_b32_e32 v143, s34, v199
	v_or_b32_e32 v142, s34, v200
	v_add_u32_e32 v0, s34, v208
	s_xor_b32 s34, s2, 1
	s_waitcnt vmcnt(2) lgkmcnt(0)
	s_barrier
	ds_read_b128 v[134:137], v201 offset:0
	s_mul_i32 s37, s34, 0xc000
	ds_read_b128 v[138:141], v202 offset:0
	ds_read_b128 v[144:147], v203 offset:0
	ds_read_b128 v[148:151], v204 offset:0
	v_add_u32_e32 v1, s37, v209
	ds_read_b128 v[152:155], v1 offset:0
	ds_read_b128 v[156:159], v1 offset:0x4000
	ds_read_b128 v[160:163], v1 offset:0x8000
	ds_read_b128 v[164:167], v1 offset:0x400
	ds_read_b128 v[168:171], v1 offset:0x4400
	ds_read_b128 v[174:177], v1 offset:0x8400
	ds_read_b128 v[178:181], v172 offset:0
	s_waitcnt lgkmcnt(10)
	v_subrev_u32_e32 v186, 56, v215
	v_mfma_f32_16x16x32_f16 v[182:185], v[2:5], v[134:137], v[118:121]
	v_min_u32_e32 v225, s17, v186
	v_add_u32_e32 v224, s20, v216
	v_mov_b32_e32 v230, s16
	v_mfma_f32_16x16x32_f16 v[186:189], v[42:45], v[134:137], v[122:125]
	v_cmp_gt_u32_e32 vcc, s8, v224
	ds_read_b128 v[226:229], v223 offset:0
	s_waitcnt lgkmcnt(10)
	v_mfma_f32_16x16x32_f16 v[134:137], v[66:69], v[134:137], v[126:129]
	v_lshl_or_b32 v173, v196, 8, v190
	v_cndmask_b32_e32 v230, v230, v224, vcc
	v_lshlrev_b32_e32 v234, 5, v230
	v_mfma_f32_16x16x32_f16 v[182:185], v[6:9], v[138:141], v[182:185]
	v_add_u32_e32 v196, -8, v215
	v_min_u32_e32 v238, s17, v196
	v_subrev_u32_e32 v196, 52, v215
	v_mfma_f32_16x16x32_f16 v[186:189], v[46:49], v[138:141], v[186:189]
	v_add_u32_e32 v221, -4, v215
	v_min_u32_e32 v196, s18, v196
	v_min_u32_e32 v221, s18, v221
	v_mfma_f32_16x16x32_f16 v[230:233], v[70:73], v[138:141], v[134:137]
	global_load_dwordx4 v[134:137], v234, s[6:7]
	global_load_dwordx4 v[138:141], v234, s[6:7] offset:16
	ds_read_b128 v[234:237], v143 offset:0
	s_waitcnt lgkmcnt(10)
	v_lshl_or_b32 v242, v192, 8, v190
	v_mfma_f32_16x16x32_f16 v[182:185], v[50:53], v[144:147], v[182:185]
	global_load_dword v192, v196, s[4:5]
	v_subrev_u32_e32 v239, 48, v215
	global_load_dword v221, v221, s[4:5]
	v_mfma_f32_16x16x32_f16 v[186:189], v[18:21], v[144:147], v[186:189]
	v_min_u32_e32 v222, s19, v215
	v_min_u32_e32 v239, s19, v239
	v_lshl_or_b32 v241, v194, 8, v191
	v_mfma_f32_16x16x32_f16 v[144:147], v[74:77], v[144:147], v[230:233]
	global_load_dword v196, v239, s[4:5]
	ds_read_b128 v[230:233], v142 offset:0
	s_waitcnt lgkmcnt(10)
	global_load_dword v194, v222, s[4:5]
	s_add_i32 s2, s28, s3
	v_mfma_f32_16x16x32_f16 v[182:185], v[10:13], v[148:151], v[182:185]
	v_lshl_or_b32 v243, v193, 8, v190
	global_load_dword v193, v225, s[4:5]
	s_min_i32 s35, s2, s14
	v_mfma_f32_16x16x32_f16 v[186:189], v[58:61], v[148:151], v[186:189]
	global_load_dword v222, v238, s[4:5]
	s_lshl_b32 s35, s35, 14
	s_lshl_b32 s34, s34, 14
	v_mfma_f32_16x16x32_f16 v[148:151], v[90:93], v[148:151], v[144:147]
	s_add_i32 s36, s33, 0
	v_add_u32_e32 v1, s35, v210
	s_add_i32 s38, s25, s34
	s_add_i32 s39, s36, s21
	s_add_i32 s40, s26, s34
	s_add_i32 s34, s36, s23
	s_add_i32 m0, s39, 0x8000
	v_add_u32_e32 v240, s35, v211
	s_add_i32 s41, s34, 0x8000
	s_add_i32 s35, s39, 0x4000
	s_add_i32 s36, s22, s33
	v_add_u32_e32 v239, s37, v212
	ds_read_b128 v[144:147], v201 offset:0x1000
	s_waitcnt lgkmcnt(4)
	s_waitcnt lgkmcnt(5)
	s_nop 0
	v_pk_add_f16 v152, v152, v156
	v_pk_add_f16 v153, v153, v157
	v_pk_add_f16 v154, v154, v158
	v_pk_add_f16 v155, v155, v159
	v_pk_add_f16 v154, v154, v162
	v_pk_add_f16 v155, v155, v163
	v_pk_add_f16 v153, v153, v161
	v_pk_add_f16 v152, v152, v160
	ds_write_b128 v239, v[152:155]
	v_pk_add_f16 v152, v164, v168
	v_pk_add_f16 v153, v165, v169
	v_pk_add_f16 v154, v166, v170
	v_pk_add_f16 v155, v167, v171
	v_pk_add_f16 v154, v154, v176
	v_pk_add_f16 v155, v155, v177
	v_pk_add_f16 v153, v153, v175
	v_pk_add_f16 v152, v152, v174
	ds_write_b128 v239, v[152:155] offset:1024
	ds_read_b128 v[152:155], v202 offset:0x1000
	s_waitcnt lgkmcnt(4)
	global_load_lds_dwordx4 v173, s[12:13]
	s_mov_b32 m0, s38
	ds_read_b128 v[168:171], v203 offset:0x1000
	s_waitcnt lgkmcnt(4)
	v_mfma_f32_16x16x32_f16 v[182:185], v[14:17], v[178:181], v[182:185]
	global_load_lds_dwordx4 v1, s[12:13]
	ds_read_b128 v[174:177], v204 offset:0x1000
	v_mfma_f32_16x16x32_f16 v[186:189], v[22:25], v[178:181], v[186:189]
	s_waitcnt lgkmcnt(4)
	v_mfma_f32_16x16x32_f16 v[178:181], v[86:89], v[178:181], v[130:133]
	v_mfma_f32_16x16x32_f16 v[156:159], v[26:29], v[226:229], v[182:185]
	v_mfma_f32_16x16x32_f16 v[160:163], v[34:37], v[226:229], v[186:189]
	v_mfma_f32_16x16x32_f16 v[164:167], v[78:81], v[226:229], v[178:181]
	v_mfma_f32_16x16x32_f16 v[156:159], v[30:33], v[234:237], v[156:159]
	v_mfma_f32_16x16x32_f16 v[160:163], v[38:41], v[234:237], v[160:163]
	v_mfma_f32_16x16x32_f16 v[164:167], v[82:85], v[234:237], v[164:167]
	v_mfma_f32_16x16x32_f16 v[156:159], v[54:57], v[230:233], v[156:159]
	v_mfma_f32_16x16x32_f16 v[160:163], v[62:65], v[230:233], v[160:163]
	v_mfma_f32_16x16x32_f16 v[164:167], v[94:97], v[230:233], v[164:167]
	s_mov_b32 m0, s41
	ds_read_b64 v[234:235], v0 offset:0
	ds_read_b128 v[178:181], v172 offset:0x1000
	s_waitcnt lgkmcnt(5)
	ds_read_b128 v[186:189], v223 offset:0x1000
	s_waitcnt lgkmcnt(5)
	s_nop 4
	v_exp_f32_e32 v1, v156
	s_waitcnt lgkmcnt(2)
	ds_read_b128 v[230:233], v143 offset:0x1000
	s_waitcnt lgkmcnt(5)
	global_load_lds_dwordx4 v241, s[12:13]
	v_add_f32_e32 v1, 1.0, v1
	v_rcp_f32_e32 v1, v1
	v_exp_f32_e32 v156, v160
	v_mfma_f32_16x16x32_f16 v[182:185], v[2:5], v[144:147], v[118:121]
	v_add_u32_e32 v225, v206, v213
	v_fma_f32 v1, v1, v164, v148
	v_exp_f32_e32 v1, v1
	v_add_f32_e32 v148, 1.0, v156
	v_exp_f32_e32 v156, v157
	v_rcp_f32_e32 v148, v148
	v_add_f32_e32 v1, 1.0, v1
	v_rcp_f32_e32 v1, v1
	v_add_f32_e32 v156, 1.0, v156
	v_rcp_f32_e32 v156, v156
	v_mfma_f32_16x16x32_f16 v[226:229], v[42:45], v[144:147], v[122:125]
	v_fma_f32 v1, v1, -2.0, 1.0
	v_fma_f32 v1, -v148, v1, v1
	v_fma_mixlo_f16 v1, v148, v234, v1 op_sel_hi:[0,1,0]
	v_mfma_f32_16x16x32_f16 v[144:147], v[66:69], v[144:147], v[126:129]
	v_exp_f32_e32 v148, v161
	v_fma_f32 v149, v156, v165, v149
	v_exp_f32_e32 v149, v149
	v_mfma_f32_16x16x32_f16 v[182:185], v[6:9], v[152:155], v[182:185]
	v_add_f32_e32 v148, 1.0, v148
	v_rcp_f32_e32 v156, v148
	v_add_f32_e32 v148, 1.0, v149
	v_mfma_f32_16x16x32_f16 v[226:229], v[46:49], v[152:155], v[226:229]
	v_rcp_f32_e32 v157, v148
	v_cmp_eq_u32_e32 vcc, s20, v214
	v_add_u32_e32 v173, 0x1000, v225
	v_mfma_f32_16x16x32_f16 v[144:147], v[70:73], v[152:155], v[144:147]
	v_cndmask_b32_e64 v1, v1, 0, vcc
	v_mfma_f32_16x16x32_f16 v[152:155], v[50:53], v[168:171], v[182:185]
	v_mfma_f32_16x16x32_f16 v[182:185], v[18:21], v[168:171], v[226:229]
	v_mfma_f32_16x16x32_f16 v[144:147], v[74:77], v[168:171], v[144:147]
	ds_read_b128 v[168:171], v142 offset:0x1000
	s_waitcnt lgkmcnt(5)
	s_nop 0
	v_mfma_f32_16x16x32_f16 v[152:155], v[10:13], v[174:177], v[152:155]
	v_mfma_f32_16x16x32_f16 v[182:185], v[58:61], v[174:177], v[182:185]
	v_mfma_f32_16x16x32_f16 v[146:149], v[90:93], v[174:177], v[144:147]
	s_nop 3
	v_fma_f32 v144, v157, -2.0, 1.0
	v_fma_f32 v144, -v156, v144, v144
	v_fma_mixlo_f16 v144, v156, v234, v144 op_sel:[0,1,0] op_sel_hi:[0,1,0]
	v_cndmask_b32_e64 v144, v144, 0, vcc
	s_mov_b32 m0, s40
	ds_read_b128 v[174:177], v201 offset:0x2000
	s_waitcnt lgkmcnt(4)
	ds_read_b128 v[226:229], v202 offset:0x2000
	s_waitcnt lgkmcnt(4)
	v_exp_f32_e32 v145, v158
	global_load_lds_dwordx4 v240, s[12:13]
	v_exp_f32_e32 v156, v162
	v_add_f32_e32 v145, 1.0, v145
	v_rcp_f32_e32 v145, v145
	v_mfma_f32_16x16x32_f16 v[152:155], v[14:17], v[178:181], v[152:155]
	v_pack_b32_f16 v144, v1, v144
	v_fma_f32 v145, v145, v166, v150
	v_add_f32_e32 v150, 1.0, v156
	v_rcp_f32_e32 v234, v150
	v_exp_f32_e32 v150, v159
	v_mfma_f32_16x16x32_f16 v[182:185], v[22:25], v[178:181], v[182:185]
	v_exp_f32_e32 v145, v145
	v_add_f32_e32 v150, 1.0, v150
	v_mfma_f32_16x16x32_f16 v[178:181], v[86:89], v[178:181], v[130:133]
	v_rcp_f32_e32 v150, v150
	v_add_f32_e32 v145, 1.0, v145
	v_rcp_f32_e32 v145, v145
	v_mfma_f32_16x16x32_f16 v[182:185], v[34:37], v[186:189], v[182:185]
	v_fmac_f32_e32 v151, v150, v167
	v_fma_f32 v145, v145, -2.0, 1.0
	v_mfma_f32_16x16x32_f16 v[178:181], v[78:81], v[186:189], v[178:181]
	v_fma_f32 v145, -v234, v145, v145
	v_fma_mixlo_f16 v145, v234, v235, v145 op_sel_hi:[0,1,0]
	v_cndmask_b32_e64 v145, v145, 0, vcc
	v_mfma_f32_16x16x32_f16 v[152:155], v[26:29], v[186:189], v[152:155]
	ds_read_b128 v[186:189], v203 offset:0x2000
	s_waitcnt lgkmcnt(4)
	ds_read_b128 v[164:167], v204 offset:0x2000
	s_waitcnt lgkmcnt(4)
	s_nop 0
	v_mfma_f32_16x16x32_f16 v[156:159], v[38:41], v[230:233], v[182:185]
	s_nop 2
	v_exp_f32_e32 v182, v163
	v_mfma_f32_16x16x32_f16 v[160:163], v[82:85], v[230:233], v[178:181]
	s_nop 2
	v_exp_f32_e32 v178, v151
	v_mfma_f32_16x16x32_f16 v[152:155], v[30:33], v[230:233], v[152:155]
	v_add_f32_e32 v179, 1.0, v182
	v_add_f32_e32 v178, 1.0, v178
	v_mfma_f32_16x16x32_f16 v[150:153], v[54:57], v[168:171], v[152:155]
	v_mfma_f32_16x16x32_f16 v[154:157], v[62:65], v[168:171], v[156:159]
	s_nop 2
	v_rcp_f32_e32 v158, v178
	v_rcp_f32_e32 v159, v179
	v_mfma_f32_16x16x32_f16 v[168:171], v[94:97], v[168:171], v[160:163]
	v_fma_f32 v158, v158, -2.0, 1.0
	v_fma_f32 v158, -v159, v158, v158
	v_fma_mixlo_f16 v158, v159, v235, v158 op_sel:[0,1,0] op_sel_hi:[0,1,0]
	v_cndmask_b32_e64 v158, v158, 0, vcc
	v_pack_b32_f16 v145, v145, v158
	global_store_dwordx2 v173, v[144:145], s[0:1] nt
	s_mov_b32 m0, s36
	ds_read_b64 v[238:239], v0 offset:0x1000
	ds_read_b128 v[178:181], v172 offset:0x2000
	s_waitcnt lgkmcnt(5)
	ds_read_b128 v[182:185], v223 offset:0x2000
	s_waitcnt lgkmcnt(5)
	v_exp_f32_e32 v1, v150
	s_waitcnt lgkmcnt(2)
	ds_read_b128 v[234:237], v143 offset:0x2000
	s_waitcnt lgkmcnt(5)
	global_load_lds_dwordx4 v243, s[12:13]
	v_add_f32_e32 v1, 1.0, v1
	v_rcp_f32_e32 v1, v1
	v_exp_f32_e32 v145, v151
	v_mfma_f32_16x16x32_f16 v[158:161], v[2:5], v[174:177], v[118:121]
	v_exp_f32_e32 v144, v154
	v_fma_f32 v1, v1, v168, v146
	v_exp_f32_e32 v1, v1
	v_mfma_f32_16x16x32_f16 v[230:233], v[42:45], v[174:177], v[122:125]
	v_add_f32_e32 v145, 1.0, v145
	v_rcp_f32_e32 v145, v145
	v_add_f32_e32 v1, 1.0, v1
	v_mfma_f32_16x16x32_f16 v[174:177], v[66:69], v[174:177], v[126:129]
	v_add_f32_e32 v144, 1.0, v144
	v_rcp_f32_e32 v1, v1
	v_rcp_f32_e32 v144, v144
	v_mfma_f32_16x16x32_f16 v[158:161], v[6:9], v[226:229], v[158:161]
	v_fma_f32 v145, v145, v169, v147
	v_exp_f32_e32 v145, v145
	v_exp_f32_e32 v146, v155
	v_mfma_f32_16x16x32_f16 v[174:177], v[70:73], v[226:229], v[174:177]
	v_fma_f32 v1, v1, -2.0, 1.0
	v_fma_f32 v1, -v144, v1, v1
	v_fma_mixlo_f16 v240, v144, v238, v1 op_sel_hi:[0,1,0]
	v_mfma_f32_16x16x32_f16 v[230:233], v[46:49], v[226:229], v[230:233]
	v_add_f32_e32 v144, 1.0, v145
	v_add_f32_e32 v1, 1.0, v146
	v_rcp_f32_e32 v150, v144
	v_mfma_f32_16x16x32_f16 v[158:161], v[50:53], v[186:189], v[158:161]
	v_rcp_f32_e32 v1, v1
	v_add_u32_e32 v173, 0x2000, v225
	v_fma_f32 v150, v150, -2.0, 1.0
	v_mfma_f32_16x16x32_f16 v[174:177], v[74:77], v[186:189], v[174:177]
	v_fma_f32 v243, -v1, v150, v150
	v_mfma_f32_16x16x32_f16 v[226:229], v[18:21], v[186:189], v[230:233]
	ds_read_b128 v[186:189], v142 offset:0x2000
	s_waitcnt lgkmcnt(5)
	s_nop 0
	v_mfma_f32_16x16x32_f16 v[158:161], v[10:13], v[164:167], v[158:161]
	v_mfma_f32_16x16x32_f16 v[144:147], v[90:93], v[164:167], v[174:177]
	v_mfma_f32_16x16x32_f16 v[226:229], v[58:61], v[164:167], v[226:229]
	s_mov_b32 m0, s35
	ds_read_b128 v[230:233], v201 offset:0x3000
	s_waitcnt lgkmcnt(4)
	v_exp_f32_e32 v150, v152
	v_mfma_f32_16x16x32_f16 v[164:167], v[14:17], v[178:181], v[158:161]
	ds_read_b128 v[160:163], v202 offset:0x3000
	s_waitcnt lgkmcnt(4)
	global_load_lds_dwordx4 v242, s[12:13]
	v_exp_f32_e32 v154, v153
	v_add_f32_e32 v150, 1.0, v150
	v_rcp_f32_e32 v150, v150
	v_mfma_f32_16x16x32_f16 v[174:177], v[22:25], v[178:181], v[226:229]
	v_add_f32_e32 v154, 1.0, v154
	v_rcp_f32_e32 v154, v154
	v_exp_f32_e32 v151, v156
	v_mfma_f32_16x16x32_f16 v[178:181], v[86:89], v[178:181], v[130:133]
	v_fma_f32 v148, v150, v170, v148
	v_exp_f32_e32 v148, v148
	v_fmac_f32_e32 v149, v154, v171
	v_mfma_f32_16x16x32_f16 v[226:229], v[26:29], v[182:185], v[164:167]
	v_exp_f32_e32 v149, v149
	v_add_f32_e32 v150, 1.0, v151
	v_rcp_f32_e32 v241, v150
	v_mfma_f32_16x16x32_f16 v[174:177], v[34:37], v[182:185], v[174:177]
	v_add_f32_e32 v148, 1.0, v148
	ds_read_b128 v[164:167], v203 offset:0x3000
	s_waitcnt lgkmcnt(4)
	v_mfma_f32_16x16x32_f16 v[178:181], v[78:81], v[182:185], v[178:181]
	v_exp_f32_e32 v155, v157
	v_rcp_f32_e32 v148, v148
	v_add_f32_e32 v149, 1.0, v149
	v_mfma_f32_16x16x32_f16 v[150:153], v[30:33], v[234:237], v[226:229]
	v_rcp_f32_e32 v149, v149
	ds_read_b128 v[168:171], v204 offset:0x3000
	s_waitcnt lgkmcnt(4)
	v_mfma_f32_16x16x32_f16 v[174:177], v[38:41], v[234:237], v[174:177]
	v_fma_f32 v148, v148, -2.0, 1.0
	v_fma_f32 v148, -v241, v148, v148
	v_fma_mixlo_f16 v241, v241, v239, v148 op_sel_hi:[0,1,0]
	v_mfma_f32_16x16x32_f16 v[178:181], v[82:85], v[234:237], v[178:181]
	v_fma_mixhi_f16 v240, v1, v238, v243 op_sel:[0,1,0] op_sel_hi:[0,1,0]
	v_mfma_f32_16x16x32_f16 v[156:159], v[54:57], v[186:189], v[150:153]
	s_nop 2
	v_add_f32_e32 v150, 1.0, v155
	v_mfma_f32_16x16x32_f16 v[152:155], v[62:65], v[186:189], v[174:177]
	s_nop 2
	v_rcp_f32_e32 v174, v150
	v_fma_f32 v175, v149, -2.0, 1.0
	v_mfma_f32_16x16x32_f16 v[148:151], v[94:97], v[186:189], v[178:181]
	v_fma_f32 v175, -v174, v175, v175
	v_fma_mixhi_f16 v241, v174, v239, v175 op_sel:[0,1,0] op_sel_hi:[0,1,0]
	global_store_dwordx2 v173, v[240:241], s[0:1] nt
	ds_read_b64 v[188:189], v0 offset:0x2000
	ds_read_b64 v[0:1], v0 offset:0x3000
	ds_read_b128 v[172:175], v172 offset:0x3000
	s_waitcnt lgkmcnt(6)
	s_andn2_b64 vcc, exec, s[10:11]
	v_mfma_f32_16x16x32_f16 v[180:183], v[2:5], v[230:233], v[118:121]
	s_waitcnt vmcnt(14)
	v_mfma_f32_16x16x32_f16 v[176:179], v[42:45], v[230:233], v[122:125]
	v_mfma_f32_16x16x32_f16 v[184:187], v[66:69], v[230:233], v[126:129]
	s_cbranch_vccnz .LBB5_11
	v_cvt_f16_f32_e32 v226, v134
	v_cvt_f16_f32_e32 v227, v135
	v_cvt_f16_f32_e32 v228, v136
	v_cvt_f16_f32_e32 v229, v137
	v_cvt_f16_f32_e32 v230, v138
	v_cvt_f16_f32_e32 v231, v139
	v_cvt_f16_f32_e32 v232, v140
	v_cvt_f16_f32_e32 v233, v141
	v_cmp_gt_i32_e32 vcc, s8, v224
	s_nop 1
	v_cndmask_b32_e32 v224, 0, v226, vcc
	v_cndmask_b32_e32 v226, 0, v227, vcc
	v_cndmask_b32_e32 v227, 0, v228, vcc
	v_cndmask_b32_e32 v234, 0, v229, vcc
	v_cndmask_b32_e32 v228, 0, v230, vcc
	v_cndmask_b32_e32 v230, 0, v231, vcc
	v_cndmask_b32_e32 v229, 0, v232, vcc
	v_cndmask_b32_e32 v231, 0, v233, vcc
	v_pack_b32_f16 v229, v229, v231
	v_pack_b32_f16 v228, v228, v230
	v_pack_b32_f16 v227, v227, v234
	v_pack_b32_f16 v226, v224, v226
	ds_write_b128 v220, v[226:229]
	s_branch .LBB5_11

.LBB6_14:
	s_and_b32 s23, s19, 0x1000
	v_or_b32_e32 v150, s23, v202
	v_cndmask_b32_e64 v150, v217, v150, s[4:5]
	s_waitcnt lgkmcnt(0)
	s_barrier
	v_add_u32_e32 v166, 0, v150
	ds_read_b128 v[150:153], v166
	ds_read_b128 v[154:157], v166 offset:1024
	ds_read_b128 v[158:161], v166 offset:3072
	ds_read_b128 v[162:165], v166 offset:2048
	s_waitcnt lgkmcnt(0)
	v_mfma_f32_16x16x32_f16 v[150:153], v[102:105], v[150:153], 0
	v_add_u32_e32 v167, 0, v203
	v_add_u32_e32 v168, 0x18000, v167
	s_mov_b32 s22, s2
	v_mfma_f32_16x16x32_f16 v[154:157], v[102:105], v[154:157], 0
	s_nop 3
	v_max_i32_e32 v151, 0, v151
	v_max_i32_e32 v150, 0, v150
	v_max_i32_e32 v153, 0, v153
	v_mfma_f32_16x16x32_f16 v[162:165], v[102:105], v[162:165], 0
	v_max_i32_e32 v152, 0, v152
	v_max_i32_e32 v155, 0, v155
	v_max_i32_e32 v154, 0, v154
	v_mfma_f32_16x16x32_f16 v[158:161], v[102:105], v[158:161], 0
	v_add_f32_e64 v150, v150, v154
	v_add_f32_e64 v151, v151, v155
	s_nop 1
	v_max_i32_e32 v155, 0, v163
	v_max_i32_e32 v154, 0, v162
	v_pk_add_f32 v[150:151], v[150:151], v[154:155]
	v_max_i32_e32 v155, 0, v157
	v_max_i32_e32 v154, 0, v156
	v_pk_add_f32 v[152:153], v[152:153], v[154:155]
	v_max_i32_e32 v155, 0, v165
	v_max_i32_e32 v154, 0, v164
	v_pk_add_f32 v[152:153], v[152:153], v[154:155]
	v_cvt_pk_f16_f32 v150, v150, v151
	v_cvt_pk_f16_f32 v151, v152, v153
	v_cvt_pk_f16_f32 v153, v160, v161
	v_pk_max_f16 v153, v153, 0
	v_cvt_pk_f16_f32 v152, v158, v159
	v_pk_max_f16 v152, v152, 0
	ds_write_b64 v167, v[150:151]
	ds_write_b64 v168, v[152:153]
	ds_read_b128 v[150:153], v166 offset:256
	ds_read_b128 v[154:157], v166 offset:1280
	ds_read_b128 v[158:161], v166 offset:2304
	ds_read_b128 v[162:165], v166 offset:3328
	s_waitcnt lgkmcnt(3)
	v_mfma_f32_16x16x32_f16 v[150:153], v[102:105], v[150:153], 0
	v_subrev_co_u32_e32 v215, vcc, 1, v215
	s_waitcnt lgkmcnt(2)
	v_mfma_f32_16x16x32_f16 v[154:157], v[102:105], v[154:157], 0
	s_nop 4
	v_max_i32_e32 v151, 0, v151
	v_max_i32_e32 v150, 0, v150
	v_max_i32_e32 v153, 0, v153
	s_waitcnt lgkmcnt(1)
	v_mfma_f32_16x16x32_f16 v[158:161], v[102:105], v[158:161], 0
	v_max_i32_e32 v152, 0, v152
	v_max_i32_e32 v155, 0, v155
	v_max_i32_e32 v154, 0, v154
	s_waitcnt lgkmcnt(0)
	v_mfma_f32_16x16x32_f16 v[162:165], v[102:105], v[162:165], 0
	v_add_f32_e64 v150, v150, v154
	v_add_f32_e64 v151, v151, v155
	s_nop 0
	v_max_i32_e32 v155, 0, v159
	v_max_i32_e32 v154, 0, v158
	v_pk_add_f32 v[150:151], v[150:151], v[154:155]
	v_max_i32_e32 v155, 0, v157
	v_max_i32_e32 v154, 0, v156
	v_pk_add_f32 v[152:153], v[152:153], v[154:155]
	v_max_i32_e32 v155, 0, v161
	v_max_i32_e32 v154, 0, v160
	v_pk_add_f32 v[152:153], v[152:153], v[154:155]
	v_cvt_pk_f16_f32 v150, v150, v151
	v_cvt_pk_f16_f32 v151, v152, v153
	v_cvt_pk_f16_f32 v153, v164, v165
	v_pk_max_f16 v153, v153, 0
	v_cvt_pk_f16_f32 v152, v162, v163
	v_pk_max_f16 v152, v152, 0
	ds_write_b64 v167, v[150:151] offset:4096
	ds_write_b64 v168, v[152:153] offset:4096
	ds_read_b128 v[150:153], v166 offset:512
	ds_read_b128 v[154:157], v166 offset:1536
	ds_read_b128 v[158:161], v166 offset:2560
	ds_read_b128 v[162:165], v166 offset:3584
	s_waitcnt lgkmcnt(3)
	v_mfma_f32_16x16x32_f16 v[150:153], v[102:105], v[150:153], 0
	s_waitcnt lgkmcnt(2)
	v_mfma_f32_16x16x32_f16 v[154:157], v[102:105], v[154:157], 0
	s_nop 5
	v_max_i32_e32 v151, 0, v151
	v_max_i32_e32 v150, 0, v150
	v_max_i32_e32 v153, 0, v153
	s_waitcnt lgkmcnt(1)
	v_mfma_f32_16x16x32_f16 v[158:161], v[102:105], v[158:161], 0
	v_max_i32_e32 v152, 0, v152
	v_max_i32_e32 v155, 0, v155
	v_max_i32_e32 v154, 0, v154
	s_waitcnt lgkmcnt(0)
	v_mfma_f32_16x16x32_f16 v[162:165], v[102:105], v[162:165], 0
	v_add_f32_e64 v150, v150, v154
	v_add_f32_e64 v151, v151, v155
	s_nop 0
	v_max_i32_e32 v155, 0, v159
	v_max_i32_e32 v154, 0, v158
	v_pk_add_f32 v[150:151], v[150:151], v[154:155]
	v_max_i32_e32 v155, 0, v157
	v_max_i32_e32 v154, 0, v156
	v_pk_add_f32 v[152:153], v[152:153], v[154:155]
	v_max_i32_e32 v155, 0, v161
	v_max_i32_e32 v154, 0, v160
	v_pk_add_f32 v[152:153], v[152:153], v[154:155]
	v_cvt_pk_f16_f32 v150, v150, v151
	v_cvt_pk_f16_f32 v151, v152, v153
	v_cvt_pk_f16_f32 v153, v164, v165
	v_pk_max_f16 v153, v153, 0
	v_cvt_pk_f16_f32 v152, v162, v163
	v_pk_max_f16 v152, v152, 0
	ds_write_b64 v167, v[150:151] offset:8192
	ds_write_b64 v168, v[152:153] offset:8192
	ds_read_b128 v[150:153], v166 offset:768
	ds_read_b128 v[154:157], v166 offset:1792
	ds_read_b128 v[158:161], v166 offset:2816
	ds_read_b128 v[162:165], v166 offset:3840
	s_waitcnt lgkmcnt(3)
	v_mfma_f32_16x16x32_f16 v[150:153], v[102:105], v[150:153], 0
	s_waitcnt lgkmcnt(2)
	v_mfma_f32_16x16x32_f16 v[154:157], v[102:105], v[154:157], 0
	s_nop 5
	v_max_i32_e32 v151, 0, v151
	v_max_i32_e32 v150, 0, v150
	v_max_i32_e32 v153, 0, v153
	s_waitcnt lgkmcnt(1)
	v_mfma_f32_16x16x32_f16 v[158:161], v[102:105], v[158:161], 0
	v_max_i32_e32 v152, 0, v152
	v_max_i32_e32 v155, 0, v155
	v_max_i32_e32 v154, 0, v154
	s_waitcnt lgkmcnt(0)
	v_mfma_f32_16x16x32_f16 v[162:165], v[102:105], v[162:165], 0
	v_add_f32_e64 v150, v150, v154
	v_add_f32_e64 v151, v151, v155
	s_nop 0
	v_max_i32_e32 v155, 0, v159
	v_max_i32_e32 v154, 0, v158
	v_pk_add_f32 v[150:151], v[150:151], v[154:155]
	v_max_i32_e32 v155, 0, v157
	v_max_i32_e32 v154, 0, v156
	v_pk_add_f32 v[152:153], v[152:153], v[154:155]
	v_max_i32_e32 v155, 0, v161
	v_max_i32_e32 v154, 0, v160
	v_pk_add_f32 v[152:153], v[152:153], v[154:155]
	v_cvt_pk_f16_f32 v150, v150, v151
	v_cvt_pk_f16_f32 v151, v152, v153
	v_cvt_pk_f16_f32 v153, v164, v165
	v_pk_max_f16 v153, v153, 0
	v_cvt_pk_f16_f32 v152, v162, v163
	v_pk_max_f16 v152, v152, 0
	ds_write_b64 v167, v[150:151] offset:12288
	ds_write_b64 v168, v[152:153] offset:12288
	s_waitcnt lgkmcnt(0)
	s_barrier
	ds_read_b128 v[150:153], v192 offset:0
	ds_read_b128 v[154:157], v192 offset:0x1000
	ds_read_b128 v[158:161], v192 offset:0x2000
	ds_read_b128 v[162:165], v192 offset:0x3000
	ds_read_b128 v[166:169], v194 offset:0
	s_nop 0
	s_waitcnt lgkmcnt(4)
	s_nop 0
	v_mfma_f32_16x16x32_f16 v[170:173], v[98:101], v[150:153], 0
	ds_read_b128 v[174:177], v194 offset:0x1000
	s_waitcnt lgkmcnt(4)
	s_nop 0
	v_mfma_f32_16x16x32_f16 v[178:181], v[98:101], v[154:157], 0
	ds_read_b128 v[182:185], v194 offset:0x2000
	s_waitcnt lgkmcnt(4)
	s_nop 0
	v_mfma_f32_16x16x32_f16 v[218:221], v[98:101], v[158:161], 0
	ds_read_b128 v[222:225], v194 offset:0x3000
	s_waitcnt lgkmcnt(4)
	s_nop 0
	v_mfma_f32_16x16x32_f16 v[226:229], v[98:101], v[162:165], 0
	ds_read_b128 v[150:153], v195 offset:0
	s_waitcnt lgkmcnt(4)
	s_nop 0
	v_mfma_f32_16x16x32_f16 v[166:169], v[110:113], v[166:169], v[170:173]
	ds_read_b128 v[154:157], v195 offset:0x1000
	s_waitcnt lgkmcnt(4)
	s_nop 0
	v_mfma_f32_16x16x32_f16 v[170:173], v[110:113], v[174:177], v[178:181]
	ds_read_b128 v[158:161], v195 offset:0x2000
	s_waitcnt lgkmcnt(4)
	s_nop 0
	v_mfma_f32_16x16x32_f16 v[174:177], v[110:113], v[182:185], v[218:221]
	ds_read_b128 v[162:165], v195 offset:0x3000
	s_waitcnt lgkmcnt(4)
	s_and_b64 vcc, exec, vcc
	v_mfma_f32_16x16x32_f16 v[178:181], v[110:113], v[222:225], v[226:229]
	s_cbranch_vccnz .LBB6_16
	v_exp_f32_e32 v142, v142
	v_exp_f32_e32 v143, v143
	v_exp_f32_e32 v138, v138
	v_exp_f32_e32 v139, v139
	v_add_f32_e32 v142, 1.0, v142
	v_rcp_f32_e32 v142, v142
	v_add_f32_e32 v143, 1.0, v143
	v_rcp_f32_e32 v143, v143
	v_add_f32_e32 v138, 1.0, v138
	v_fmac_f32_e32 v134, v146, v142
	v_exp_f32_e32 v142, v134
	v_fmac_f32_e32 v135, v147, v143
	v_exp_f32_e32 v143, v135
	v_rcp_f32_e32 v134, v138
	v_add_f32_e32 v135, 1.0, v142
	v_rcp_f32_e32 v138, v135
	v_add_f32_e32 v135, 1.0, v139
	v_add_f32_e32 v139, 1.0, v143
	v_rcp_f32_e32 v139, v139
	v_cvt_f32_f16_sdwa v143, v0 dst_sel:DWORD dst_unused:UNUSED_PAD src0_sel:WORD_1
	v_cvt_f32_f16_e32 v142, v0
	v_exp_f32_e32 v0, v144
	v_rcp_f32_e32 v135, v135
	v_pk_fma_f32 v[138:139], v[138:139], 2.0, 1.0 op_sel_hi:[1,0,0] neg_lo:[1,0,0] neg_hi:[1,0,0]
	v_exp_f32_e32 v140, v140
	v_add_f32_e32 v0, 1.0, v0
	v_pk_fma_f32 v[138:139], v[134:135], v[138:139], v[138:139] neg_lo:[1,0,0] neg_hi:[1,0,0]
	v_rcp_f32_e32 v0, v0
	v_pk_fma_f32 v[134:135], v[134:135], v[142:143], v[138:139]
	v_exp_f32_e32 v138, v145
	v_add_f32_e32 v139, 1.0, v140
	v_fmac_f32_e32 v136, v148, v0
	v_exp_f32_e32 v0, v136
	v_add_f32_e32 v136, 1.0, v138
	v_rcp_f32_e32 v138, v136
	v_rcp_f32_e32 v136, v139
	v_exp_f32_e32 v139, v141
	v_add_f32_e32 v0, 1.0, v0
	v_fmac_f32_e32 v137, v149, v138
	v_exp_f32_e32 v140, v137
	v_rcp_f32_e32 v138, v0
	v_add_f32_e32 v0, 1.0, v139
	v_rcp_f32_e32 v137, v0
	v_add_f32_e32 v0, 1.0, v140
	v_rcp_f32_e32 v139, v0
	v_cvt_f32_f16_sdwa v141, v1 dst_sel:DWORD dst_unused:UNUSED_PAD src0_sel:WORD_1
	v_cvt_f32_f16_e32 v140, v1
	v_cvt_pk_f16_f32 v0, v134, v135
	v_pk_fma_f32 v[134:135], v[138:139], 2.0, 1.0 op_sel_hi:[1,0,0] neg_lo:[1,0,0] neg_hi:[1,0,0]
	s_nop 0
	v_pk_fma_f32 v[134:135], v[136:137], v[134:135], v[134:135] neg_lo:[1,0,0] neg_hi:[1,0,0]
	s_nop 0
	v_pk_fma_f32 v[134:135], v[136:137], v[140:141], v[134:135]
	s_nop 0
	v_cvt_pk_f16_f32 v1, v134, v135
	v_add_u32_e32 v134, v193, v214
	global_store_dwordx2 v134, v[0:1], s[0:1] nt
.LBB6_16:
	v_or_b32_e32 v0, s23, v201
	v_cndmask_b32_e64 v0, v217, v0, s[4:5]
	ds_read_b128 v[134:137], v196 offset:0
	s_waitcnt lgkmcnt(4)
	s_nop 0
	v_mfma_f32_16x16x32_f16 v[138:141], v[114:117], v[150:153], v[166:169]
	ds_read_b128 v[142:145], v196 offset:0x1000
	s_waitcnt lgkmcnt(4)
	s_nop 0
	v_mfma_f32_16x16x32_f16 v[146:149], v[114:117], v[154:157], v[170:173]
	ds_read_b128 v[150:153], v196 offset:0x2000
	s_waitcnt lgkmcnt(4)
	s_nop 0
	v_mfma_f32_16x16x32_f16 v[154:157], v[114:117], v[158:161], v[174:177]
	ds_read_b128 v[158:161], v196 offset:0x3000
	s_waitcnt lgkmcnt(4)
	s_nop 0
	v_mfma_f32_16x16x32_f16 v[162:165], v[114:117], v[162:165], v[178:181]
	ds_read_b128 v[166:169], v0 offset:0
	s_waitcnt lgkmcnt(4)
	s_nop 0
	v_mfma_f32_16x16x32_f16 v[134:137], v[106:109], v[134:137], v[138:141]
	ds_read_b128 v[138:141], v0 offset:0x100
	s_waitcnt lgkmcnt(4)
	s_nop 0
	v_mfma_f32_16x16x32_f16 v[142:145], v[106:109], v[142:145], v[146:149]
	ds_read_b128 v[146:149], v0 offset:0x200
	s_waitcnt lgkmcnt(4)
	s_nop 0
	v_mfma_f32_16x16x32_f16 v[150:153], v[106:109], v[150:153], v[154:157]
	ds_read_b128 v[154:157], v0 offset:0x300
	s_waitcnt lgkmcnt(4)
	s_nop 0
	v_mfma_f32_16x16x32_f16 v[158:161], v[106:109], v[158:161], v[162:165]
	s_waitcnt lgkmcnt(3)
	s_nop 0
	v_mfma_f32_16x16x32_f16 v[134:137], v[102:105], v[166:169], v[134:137]
	s_waitcnt lgkmcnt(2)
	s_nop 0
	v_mfma_f32_16x16x32_f16 v[138:141], v[102:105], v[138:141], v[142:145]
	s_waitcnt lgkmcnt(1)
	s_nop 0
	v_mfma_f32_16x16x32_f16 v[142:145], v[102:105], v[146:149], v[150:153]
	s_waitcnt lgkmcnt(0)
	s_nop 0
	v_mfma_f32_16x16x32_f16 v[146:149], v[102:105], v[154:157], v[158:161]
	s_nop 1
	v_cvt_pk_f16_f32 v1, v136, v137
	v_pk_max_f16 v1, v1, 0
	v_cvt_pk_f16_f32 v0, v134, v135
	v_pk_max_f16 v0, v0, 0
	v_cvt_pk_f16_f32 v135, v140, v141
	v_pk_max_f16 v135, v135, 0
	v_cvt_pk_f16_f32 v134, v138, v139
	v_pk_max_f16 v134, v134, 0
	ds_write2st64_b64 v216, v[0:1], v[134:135] offset1:8
	v_cvt_pk_f16_f32 v1, v144, v145
	v_pk_max_f16 v1, v1, 0
	v_cvt_pk_f16_f32 v0, v142, v143
	v_pk_max_f16 v0, v0, 0
	v_cvt_pk_f16_f32 v135, v148, v149
	v_pk_max_f16 v135, v135, 0
	v_cvt_pk_f16_f32 v134, v146, v147
	v_pk_max_f16 v134, v134, 0
	ds_write2st64_b64 v216, v[0:1], v[134:135] offset0:16 offset1:24
	s_waitcnt lgkmcnt(0)
	s_barrier
	ds_read_b128 v[134:137], v197 offset:0
	ds_read_b128 v[138:141], v198 offset:0
	ds_read_b128 v[142:145], v199 offset:0
	ds_read_b128 v[146:149], v200 offset:0
	ds_read_b128 v[150:153], v206 offset:0
	v_add_u32_e32 v0, s16, v213
	s_waitcnt lgkmcnt(4)
	v_min_i32_e32 v0, s11, v0
	v_mfma_f32_16x16x32_f16 v[154:157], v[2:5], v[134:137], v[118:121]
	v_cndmask_b32_e64 v0, v190, v0, s[8:9]
	v_ashrrev_i32_e32 v1, 31, v0
	ds_read_b128 v[162:165], v207 offset:0
	v_mfma_f32_16x16x32_f16 v[158:161], v[42:45], v[134:137], v[122:125]
	s_waitcnt lgkmcnt(4)
	v_lshlrev_b64 v[0:1], 5, v[0:1]
	v_lshl_add_u64 v[0:1], s[14:15], 0, v[0:1]
	v_mfma_f32_16x16x32_f16 v[134:137], v[66:69], v[134:137], v[126:129]
	v_lshl_add_u64 v[170:171], v[0:1], 0, 16
	v_mfma_f32_16x16x32_f16 v[154:157], v[6:9], v[138:141], v[154:157]
	v_mfma_f32_16x16x32_f16 v[158:161], v[46:49], v[138:141], v[158:161]
	v_mfma_f32_16x16x32_f16 v[166:169], v[70:73], v[138:141], v[134:137]
	global_load_dwordx4 v[138:141], v[0:1], off
	global_load_dwordx4 v[134:137], v[170:171], off
	ds_read_b128 v[170:173], v208 offset:0
	s_waitcnt lgkmcnt(4)
	v_add_u32_e32 v0, s16, v212
	v_mfma_f32_16x16x32_f16 v[154:157], v[50:53], v[142:145], v[154:157]
	v_min_i32_e32 v0, s11, v0
	v_mad_i64_i32 v[0:1], s[2:3], v0, 12, s[12:13]
	v_mfma_f32_16x16x32_f16 v[158:161], v[18:21], v[142:145], v[158:161]
	v_lshl_add_u64 v[0:1], v[0:1], 0, v[186:187]
	global_load_dword v190, v[0:1], off
	v_mfma_f32_16x16x32_f16 v[142:145], v[74:77], v[142:145], v[166:169]
	ds_read_b128 v[166:169], v209 offset:0
	s_waitcnt lgkmcnt(4)
	s_nop 0
	v_mfma_f32_16x16x32_f16 v[154:157], v[10:13], v[146:149], v[154:157]
	v_mfma_f32_16x16x32_f16 v[158:161], v[58:61], v[146:149], v[158:161]
	v_mfma_f32_16x16x32_f16 v[146:149], v[90:93], v[146:149], v[142:145]
	ds_read_b128 v[142:145], v197 offset:0x1000
	s_waitcnt lgkmcnt(4)
	ds_read_b128 v[174:177], v198 offset:0x1000
	s_waitcnt lgkmcnt(4)
	s_nop 0
	v_mfma_f32_16x16x32_f16 v[154:157], v[14:17], v[150:153], v[154:157]
	v_mfma_f32_16x16x32_f16 v[158:161], v[22:25], v[150:153], v[158:161]
	v_mfma_f32_16x16x32_f16 v[150:153], v[86:89], v[150:153], v[130:133]
	v_mfma_f32_16x16x32_f16 v[154:157], v[26:29], v[162:165], v[154:157]
	v_mfma_f32_16x16x32_f16 v[158:161], v[34:37], v[162:165], v[158:161]
	v_mfma_f32_16x16x32_f16 v[150:153], v[78:81], v[162:165], v[150:153]
	ds_read_b128 v[162:165], v199 offset:0x1000
	s_waitcnt lgkmcnt(4)
	s_nop 0
	v_mfma_f32_16x16x32_f16 v[154:157], v[30:33], v[170:173], v[154:157]
	v_mfma_f32_16x16x32_f16 v[158:161], v[38:41], v[170:173], v[158:161]
	v_mfma_f32_16x16x32_f16 v[150:153], v[82:85], v[170:173], v[150:153]
	ds_read_b128 v[170:173], v200 offset:0x1000
	s_waitcnt lgkmcnt(4)
	s_nop 0
	v_mfma_f32_16x16x32_f16 v[154:157], v[54:57], v[166:169], v[154:157]
	v_mfma_f32_16x16x32_f16 v[158:161], v[62:65], v[166:169], v[158:161]
	v_mfma_f32_16x16x32_f16 v[150:153], v[94:97], v[166:169], v[150:153]
	s_nop 5
	v_exp_f32_e32 v154, v154
	v_exp_f32_e32 v158, v158
	ds_read_b64 v[0:1], v204 offset:0
	ds_read_b128 v[166:169], v206 offset:0x1000
	v_add_f32_e32 v154, 1.0, v154
	v_rcp_f32_e32 v154, v154
	v_add_f32_e32 v158, 1.0, v158
	s_waitcnt lgkmcnt(5)
	ds_read_b128 v[220:223], v207 offset:0x1000
	v_fma_f32 v146, v154, v150, v146
	v_exp_f32_e32 v146, v146
	v_exp_f32_e32 v154, v155
	v_rcp_f32_e32 v150, v158
	v_mfma_f32_16x16x32_f16 v[178:181], v[2:5], v[142:145], v[118:121]
	v_add_f32_e32 v146, 1.0, v146
	v_add_f32_e32 v154, 1.0, v154
	v_rcp_f32_e32 v146, v146
	v_rcp_f32_e32 v154, v154
	v_mfma_f32_16x16x32_f16 v[182:185], v[42:45], v[142:145], v[122:125]
	s_waitcnt lgkmcnt(5)
	v_fma_f32 v146, v146, -2.0, 1.0
	v_fma_f32 v147, v154, v151, v147
	v_mfma_f32_16x16x32_f16 v[142:145], v[66:69], v[142:145], v[126:129]
	v_fma_f32 v146, -v150, v146, v146
	v_exp_f32_e32 v147, v147
	s_waitcnt lgkmcnt(2)
	v_mfma_f32_16x16x32_f16 v[178:181], v[6:9], v[174:177], v[178:181]
	v_fma_mixlo_f16 v146, v150, v0, v146 op_sel_hi:[0,1,0]
	v_exp_f32_e32 v150, v159
	v_add_f32_e32 v147, 1.0, v147
	v_mfma_f32_16x16x32_f16 v[182:185], v[46:49], v[174:177], v[182:185]
	v_rcp_f32_e32 v151, v147
	v_add_f32_e32 v150, 1.0, v150
	v_rcp_f32_e32 v150, v150
	v_mfma_f32_16x16x32_f16 v[142:145], v[70:73], v[174:177], v[142:145]
	ds_read_b128 v[174:177], v208 offset:0x1000
	s_waitcnt lgkmcnt(5)
	v_cmp_eq_u32_e32 vcc, s16, v211
	v_mfma_f32_16x16x32_f16 v[178:181], v[50:53], v[162:165], v[178:181]
	v_add_u32_e32 v218, v193, v210
	v_cndmask_b32_e64 v189, v146, 0, vcc
	v_add_u32_e32 v188, 0x1000, v218
	v_mfma_f32_16x16x32_f16 v[182:185], v[18:21], v[162:165], v[182:185]
	v_mfma_f32_16x16x32_f16 v[142:145], v[74:77], v[162:165], v[142:145]
	ds_read_b128 v[162:165], v209 offset:0x1000
	s_waitcnt lgkmcnt(5)
	s_nop 0
	v_mfma_f32_16x16x32_f16 v[178:181], v[10:13], v[170:173], v[178:181]
	v_mfma_f32_16x16x32_f16 v[182:185], v[58:61], v[170:173], v[182:185]
	v_mfma_f32_16x16x32_f16 v[144:147], v[90:93], v[170:173], v[142:145]
	s_nop 3
	v_fma_f32 v142, v151, -2.0, 1.0
	v_fma_f32 v142, -v150, v142, v142
	v_fma_mixlo_f16 v0, v150, v0, v142 op_sel:[0,1,0] op_sel_hi:[0,1,0]
	v_cndmask_b32_e64 v0, v0, 0, vcc
	v_exp_f32_e32 v142, v156
	ds_read_b128 v[170:173], v197 offset:0x2000
	s_waitcnt lgkmcnt(4)
	v_exp_f32_e32 v143, v160
	v_add_f32_e32 v142, 1.0, v142
	v_rcp_f32_e32 v142, v142
	v_mfma_f32_16x16x32_f16 v[182:185], v[22:25], v[166:169], v[182:185]
	ds_read_b128 v[224:227], v198 offset:0x2000
	s_waitcnt lgkmcnt(4)
	v_fma_f32 v142, v142, v152, v148
	v_exp_f32_e32 v148, v157
	v_mfma_f32_16x16x32_f16 v[178:181], v[14:17], v[166:169], v[178:181]
	v_exp_f32_e32 v142, v142
	v_add_f32_e32 v143, 1.0, v143
	v_add_f32_e32 v148, 1.0, v148
	v_rcp_f32_e32 v148, v148
	v_mfma_f32_16x16x32_f16 v[166:169], v[86:89], v[166:169], v[130:133]
	v_add_f32_e32 v142, 1.0, v142
	v_rcp_f32_e32 v142, v142
	v_rcp_f32_e32 v143, v143
	v_mfma_f32_16x16x32_f16 v[182:185], v[34:37], v[220:223], v[182:185]
	v_fmac_f32_e32 v149, v148, v153
	v_exp_f32_e32 v150, v161
	v_fma_f32 v142, v142, -2.0, 1.0
	v_mfma_f32_16x16x32_f16 v[178:181], v[26:29], v[220:223], v[178:181]
	v_fma_f32 v142, -v143, v142, v142
	v_fma_mixlo_f16 v142, v143, v1, v142 op_sel_hi:[0,1,0]
	v_add_f32_e32 v143, 1.0, v150
	v_mfma_f32_16x16x32_f16 v[154:157], v[78:81], v[220:223], v[166:169]
	ds_read_b128 v[166:169], v199 offset:0x2000
	s_waitcnt lgkmcnt(4)
	v_rcp_f32_e32 v143, v143
	v_mfma_f32_16x16x32_f16 v[158:161], v[38:41], v[174:177], v[182:185]
	v_cndmask_b32_e64 v142, v142, 0, vcc
	v_pack_b32_f16 v0, v189, v0
	s_nop 0
	v_exp_f32_e32 v182, v149
	v_mfma_f32_16x16x32_f16 v[178:181], v[30:33], v[174:177], v[178:181]
	v_mfma_f32_16x16x32_f16 v[148:151], v[82:85], v[174:177], v[154:157]
	ds_read_b128 v[152:155], v200 offset:0x2000
	s_waitcnt lgkmcnt(4)
	s_nop 0
	v_mfma_f32_16x16x32_f16 v[174:177], v[54:57], v[162:165], v[178:181]
	s_nop 0
	v_add_f32_e32 v156, 1.0, v182
	s_nop 2
	v_rcp_f32_e32 v178, v156
	v_mfma_f32_16x16x32_f16 v[156:159], v[62:65], v[162:165], v[158:161]
	s_nop 2
	v_fma_f32 v160, v178, -2.0, 1.0
	v_fma_f32 v160, -v143, v160, v160
	v_mfma_f32_16x16x32_f16 v[148:151], v[94:97], v[162:165], v[148:151]
	v_fma_mixlo_f16 v1, v143, v1, v160 op_sel:[0,1,0] op_sel_hi:[0,1,0]
	v_cndmask_b32_e64 v1, v1, 0, vcc
	v_pack_b32_f16 v1, v142, v1
	global_store_dwordx2 v188, v[0:1], s[0:1] nt
	v_exp_f32_e32 v142, v174
	v_exp_f32_e32 v143, v156
	ds_read_b64 v[0:1], v204 offset:0x1000
	ds_read_b128 v[160:163], v206 offset:0x2000
	v_add_f32_e32 v142, 1.0, v142
	v_rcp_f32_e32 v142, v142
	s_waitcnt lgkmcnt(5)
	v_add_f32_e32 v143, 1.0, v143
	v_mfma_f32_16x16x32_f16 v[178:181], v[2:5], v[170:173], v[118:121]
	v_fma_f32 v142, v142, v148, v144
	v_exp_f32_e32 v144, v175
	v_exp_f32_e32 v142, v142
	v_mfma_f32_16x16x32_f16 v[182:185], v[42:45], v[170:173], v[122:125]
	v_rcp_f32_e32 v143, v143
	v_add_f32_e32 v144, 1.0, v144
	v_add_f32_e32 v142, 1.0, v142
	v_mfma_f32_16x16x32_f16 v[170:173], v[66:69], v[170:173], v[126:129]
	v_rcp_f32_e32 v144, v144
	v_rcp_f32_e32 v142, v142
	ds_read_b128 v[220:223], v207 offset:0x2000
	s_waitcnt lgkmcnt(5)
	v_fma_f32 v148, v144, v149, v145
	v_mfma_f32_16x16x32_f16 v[178:181], v[6:9], v[224:227], v[178:181]
	v_fma_f32 v142, v142, -2.0, 1.0
	v_exp_f32_e32 v148, v148
	v_fma_f32 v142, -v143, v142, v142
	v_mfma_f32_16x16x32_f16 v[182:185], v[46:49], v[224:227], v[182:185]
	v_exp_f32_e32 v149, v157
	s_waitcnt lgkmcnt(2)
	v_add_f32_e32 v148, 1.0, v148
	v_mfma_f32_16x16x32_f16 v[170:173], v[70:73], v[224:227], v[170:173]
	ds_read_b128 v[224:227], v208 offset:0x2000
	s_waitcnt lgkmcnt(5)
	v_fma_mixlo_f16 v188, v143, v0, v142 op_sel_hi:[0,1,0]
	v_mfma_f32_16x16x32_f16 v[178:181], v[50:53], v[166:169], v[178:181]
	v_rcp_f32_e32 v148, v148
	v_add_f32_e32 v149, 1.0, v149
	v_rcp_f32_e32 v232, v149
	v_mfma_f32_16x16x32_f16 v[182:185], v[18:21], v[166:169], v[182:185]
	v_fma_f32 v148, v148, -2.0, 1.0
	v_add_u32_e32 v219, 0x2000, v218
	v_fma_f32 v233, -v232, v148, v148
	v_mfma_f32_16x16x32_f16 v[142:145], v[74:77], v[166:169], v[170:173]
	ds_read_b128 v[170:173], v209 offset:0x2000
	s_waitcnt lgkmcnt(5)
	s_nop 0
	v_mfma_f32_16x16x32_f16 v[164:167], v[10:13], v[152:155], v[178:181]
	v_mfma_f32_16x16x32_f16 v[178:181], v[58:61], v[152:155], v[182:185]
	v_mfma_f32_16x16x32_f16 v[142:145], v[90:93], v[152:155], v[142:145]
	v_exp_f32_e32 v148, v176
	v_exp_f32_e32 v149, v158
	ds_read_b128 v[228:231], v197 offset:0x3000
	s_waitcnt lgkmcnt(4)
	v_add_f32_e32 v148, 1.0, v148
	v_rcp_f32_e32 v148, v148
	v_mfma_f32_16x16x32_f16 v[152:155], v[14:17], v[160:163], v[164:167]
	v_fma_mixhi_f16 v188, v232, v0, v233 op_sel:[0,1,0] op_sel_hi:[0,1,0]
	v_fma_f32 v146, v148, v150, v146
	v_add_f32_e32 v148, 1.0, v149
	v_exp_f32_e32 v149, v177
	v_mfma_f32_16x16x32_f16 v[166:169], v[22:25], v[160:163], v[178:181]
	v_exp_f32_e32 v146, v146
	v_exp_f32_e32 v150, v159
	v_add_f32_e32 v149, 1.0, v149
	v_rcp_f32_e32 v149, v149
	v_mfma_f32_16x16x32_f16 v[178:181], v[86:89], v[160:163], v[130:133]
	ds_read_b128 v[162:165], v198 offset:0x3000
	s_waitcnt lgkmcnt(4)
	v_fmac_f32_e32 v147, v149, v151
	v_exp_f32_e32 v147, v147
	v_add_f32_e32 v146, 1.0, v146
	v_mfma_f32_16x16x32_f16 v[152:155], v[26:29], v[220:223], v[152:155]
	v_rcp_f32_e32 v146, v146
	v_add_f32_e32 v147, 1.0, v147
	v_rcp_f32_e32 v148, v148
	v_mfma_f32_16x16x32_f16 v[182:185], v[34:37], v[220:223], v[166:169]
	v_add_f32_e32 v150, 1.0, v150
	v_rcp_f32_e32 v147, v147
	v_rcp_f32_e32 v150, v150
	v_mfma_f32_16x16x32_f16 v[174:177], v[78:81], v[220:223], v[178:181]
	ds_read_b128 v[166:169], v199 offset:0x3000
	s_waitcnt lgkmcnt(4)
	v_fma_f32 v146, v146, -2.0, 1.0
	v_mfma_f32_16x16x32_f16 v[152:155], v[30:33], v[224:227], v[152:155]
	v_fma_f32 v146, -v148, v146, v146
	v_fma_f32 v151, v147, -2.0, 1.0
	v_fma_mixlo_f16 v189, v148, v1, v146 op_sel_hi:[0,1,0]
	v_mfma_f32_16x16x32_f16 v[178:181], v[38:41], v[224:227], v[182:185]
	v_fma_f32 v151, -v150, v151, v151
	ds_read_b128 v[158:161], v200 offset:0x3000
	s_waitcnt lgkmcnt(4)
	v_mfma_f32_16x16x32_f16 v[174:177], v[82:85], v[224:227], v[174:177]
	v_fma_mixhi_f16 v189, v150, v1, v151 op_sel:[0,1,0] op_sel_hi:[0,1,0]
	global_store_dwordx2 v219, v[188:189], s[0:1] nt
	v_mfma_f32_16x16x32_f16 v[154:157], v[54:57], v[170:173], v[152:155]
	v_mfma_f32_16x16x32_f16 v[146:149], v[62:65], v[170:173], v[178:181]
	v_mfma_f32_16x16x32_f16 v[150:153], v[94:97], v[170:173], v[174:177]
	ds_read_b64 v[188:189], v204 offset:0x2000
	ds_read_b64 v[0:1], v204 offset:0x3000
	ds_read_b128 v[170:173], v206 offset:0x3000
	s_waitcnt lgkmcnt(6)
	s_waitcnt vmcnt(2)
	s_nop 0
	v_mfma_f32_16x16x32_f16 v[182:185], v[2:5], v[228:231], v[118:121]
	v_mfma_f32_16x16x32_f16 v[174:177], v[42:45], v[228:231], v[122:125]
	v_mfma_f32_16x16x32_f16 v[178:181], v[66:69], v[228:231], v[126:129]
	s_and_saveexec_b64 s[2:3], s[6:7]
	s_cbranch_execz .LBB6_13
	s_xor_b32 s23, s23, 0x1000
	v_cvt_pk_f16_f32 v221, v140, v141
	v_cvt_pk_f16_f32 v220, v138, v139
	v_cvt_pk_f16_f32 v223, v136, v137
	v_cvt_pk_f16_f32 v222, v134, v135
	v_add_u32_e32 v134, s23, v205
	ds_write_b128 v134, v[220:223] offset:49152
	s_branch .LBB6_13

.LBB8_5:
	v_add_u32_e32 v22, s18, v47
	v_mov_b32_e32 v23, s14
	v_cmp_gt_u32_e32 vcc, s12, v22
	s_waitcnt lgkmcnt(0)
	s_barrier
	v_add_u32_e32 v56, -4, v46
	v_min_u32_e32 v56, s16, v56
	v_cndmask_b32_e32 v22, v23, v22, vcc
	v_lshlrev_b32_e32 v27, 4, v22
	global_load_dwordx4 v[22:25], v27, s[10:11]
	global_load_dwordx4 v[52:55], v27, s[10:11]
	v_subrev_u32_e32 v27, 52, v46
	v_min_u32_e32 v27, s16, v27
	global_load_dword v27, v27, s[8:9]
	global_load_dword v92, v56, s[8:9]
	v_subrev_u32_e32 v56, 48, v46
	v_min_u32_e32 v56, s17, v56
	global_load_dword v93, v56, s[8:9]
	v_min_u32_e32 v56, s17, v46
	global_load_dword v94, v56, s[8:9]
	v_subrev_u32_e32 v56, 56, v46
	v_min_u32_e32 v56, s15, v56
	global_load_dword v95, v56, s[8:9]
	v_add_u32_e32 v56, -8, v46
	s_add_i32 s25, s24, s19
	v_min_u32_e32 v56, s15, v56
	global_load_dword v96, v56, s[8:9]
	v_lshl_or_b32 v50, v50, 8, v29
	s_add_i32 m0, s25, 0x4000
	s_add_i32 s24, s24, s20
	global_load_lds_dwordx4 v50, s[4:5]
	v_lshl_or_b32 v50, v51, 8, v31
	s_add_i32 m0, s24, 0x4000
	s_add_i32 s2, s2, s3
	global_load_lds_dwordx4 v50, s[4:5]
	v_or_b32_e32 v50, s23, v32
	v_or_b32_e32 v51, s23, v33
	v_or_b32_e32 v97, s23, v34
	v_or_b32_e32 v98, s23, v35
	ds_read_b128 v[56:59], v50 offset:0
	ds_read_b128 v[60:63], v50 offset:0x1000
	ds_read_b128 v[64:67], v50 offset:0x2000
	ds_read_b128 v[68:71], v50 offset:0x3000
	ds_read_b128 v[72:75], v51 offset:0
	s_nop 0
	s_waitcnt lgkmcnt(4)
	s_nop 0
	v_mfma_f32_16x16x32_f16 v[56:59], v[14:17], v[56:59], 0
	ds_read_b128 v[76:79], v51 offset:0x1000
	s_waitcnt lgkmcnt(4)
	s_nop 0
	v_mfma_f32_16x16x32_f16 v[60:63], v[14:17], v[60:63], 0
	ds_read_b128 v[80:83], v51 offset:0x2000
	s_waitcnt lgkmcnt(4)
	s_nop 0
	v_mfma_f32_16x16x32_f16 v[64:67], v[14:17], v[64:67], 0
	ds_read_b128 v[84:87], v51 offset:0x3000
	s_waitcnt lgkmcnt(4)
	s_nop 0
	v_mfma_f32_16x16x32_f16 v[68:71], v[14:17], v[68:71], 0
	ds_read_b128 v[88:91], v97 offset:0
	s_waitcnt lgkmcnt(4)
	s_nop 0
	v_mfma_f32_16x16x32_f16 v[56:59], v[2:5], v[72:75], v[56:59]
	ds_read_b128 v[72:75], v97 offset:0x1000
	s_waitcnt lgkmcnt(4)
	s_nop 0
	v_mfma_f32_16x16x32_f16 v[60:63], v[2:5], v[76:79], v[60:63]
	ds_read_b128 v[76:79], v97 offset:0x2000
	s_waitcnt lgkmcnt(4)
	s_nop 0
	v_mfma_f32_16x16x32_f16 v[64:67], v[2:5], v[80:83], v[64:67]
	ds_read_b128 v[80:83], v97 offset:0x3000
	s_waitcnt lgkmcnt(4)
	s_nop 0
	v_mfma_f32_16x16x32_f16 v[68:71], v[2:5], v[84:87], v[68:71]
	ds_read_b128 v[84:87], v98 offset:0
	s_waitcnt lgkmcnt(4)
	s_nop 0
	v_mfma_f32_16x16x32_f16 v[56:59], v[6:9], v[88:91], v[56:59]
	ds_read_b128 v[88:91], v98 offset:0x1000
	s_waitcnt lgkmcnt(4)
	s_nop 0
	v_mfma_f32_16x16x32_f16 v[60:63], v[6:9], v[72:75], v[60:63]
	ds_read_b128 v[72:75], v98 offset:0x2000
	s_waitcnt lgkmcnt(4)
	s_nop 0
	v_mfma_f32_16x16x32_f16 v[64:67], v[6:9], v[76:79], v[64:67]
	ds_read_b128 v[76:79], v98 offset:0x3000
	s_waitcnt lgkmcnt(4)
	s_nop 0
	v_mfma_f32_16x16x32_f16 v[68:71], v[6:9], v[80:83], v[68:71]
	ds_read_b128 v[80:83], v37 offset:0
	s_waitcnt lgkmcnt(4)
	s_nop 0
	v_mfma_f32_16x16x32_f16 v[56:59], v[10:13], v[84:87], v[56:59]
	ds_read_b128 v[84:87], v37 offset:0x100
	s_waitcnt lgkmcnt(4)
	s_nop 0
	v_mfma_f32_16x16x32_f16 v[60:63], v[10:13], v[88:91], v[60:63]
	ds_read_b128 v[88:91], v37 offset:0x200
	s_waitcnt lgkmcnt(4)
	s_nop 0
	v_mfma_f32_16x16x32_f16 v[64:67], v[10:13], v[72:75], v[64:67]
	ds_read_b128 v[72:75], v37 offset:0x300
	s_waitcnt lgkmcnt(4)
	s_nop 0
	v_mfma_f32_16x16x32_f16 v[68:71], v[10:13], v[76:79], v[68:71]
	s_waitcnt lgkmcnt(3)
	s_nop 0
	v_mfma_f32_16x16x32_f16 v[56:59], v[18:21], v[80:83], v[56:59]
	s_waitcnt lgkmcnt(2)
	s_nop 0
	v_mfma_f32_16x16x32_f16 v[60:63], v[18:21], v[84:87], v[60:63]
	s_waitcnt lgkmcnt(1)
	s_nop 0
	v_mfma_f32_16x16x32_f16 v[64:67], v[18:21], v[88:91], v[64:67]
	s_waitcnt lgkmcnt(0)
	s_nop 0
	v_mfma_f32_16x16x32_f16 v[68:71], v[18:21], v[72:75], v[68:71]
	s_nop 1
	v_cvt_pk_f16_f32 v51, v58, v59
	v_pk_max_f16 v51, v51, 0
	v_cvt_pk_f16_f32 v50, v56, v57
	v_pk_max_f16 v50, v50, 0
	v_cvt_pk_f16_f32 v57, v62, v63
	v_pk_max_f16 v57, v57, 0
	v_cvt_pk_f16_f32 v56, v60, v61
	v_pk_max_f16 v56, v56, 0
	ds_write2st64_b64 v48, v[50:51], v[56:57] offset1:8
	v_cvt_pk_f16_f32 v51, v66, v67
	v_pk_max_f16 v51, v51, 0
	v_cvt_pk_f16_f32 v50, v64, v65
	v_pk_max_f16 v50, v50, 0
	v_cvt_pk_f16_f32 v57, v70, v71
	v_pk_max_f16 v57, v57, 0
	v_cvt_pk_f16_f32 v56, v68, v69
	v_pk_max_f16 v56, v56, 0
	ds_write2st64_b64 v48, v[50:51], v[56:57] offset0:16 offset1:24
	s_waitcnt lgkmcnt(0)
	s_barrier
	v_lshl_or_b32 v40, v40, 8, v29
	s_add_i32 m0, s25, 0x8000
	s_xor_b64 s[6:7], s[6:7], -1
	global_load_lds_dwordx4 v40, s[4:5]
	v_lshl_or_b32 v40, v41, 8, v31
	s_add_i32 m0, s24, 0x8000
	v_add_u32_e32 v46, s22, v46
	global_load_lds_dwordx4 v40, s[4:5]
	v_lshl_or_b32 v40, v42, 8, v29
	s_mov_b32 m0, s25
	s_nop 0
	global_load_lds_dwordx4 v40, s[4:5]
	v_lshl_or_b32 v40, v45, 8, v31
	s_mov_b32 m0, s24
	s_nop 0
	global_load_lds_dwordx4 v40, s[4:5]
	v_add_u32_e32 v40, v39, v43
	ds_read_b128 v[56:59], v40
	ds_read_b128 v[60:63], v49
	v_add_u32_e32 v40, s18, v38
	v_ashrrev_i32_e32 v41, 31, v40
	v_lshlrev_b64 v[50:51], 8, v[40:41]
	v_add_u32_e32 v40, 32, v40
	v_ashrrev_i32_e32 v41, 31, v40
	v_lshlrev_b64 v[40:41], 8, v[40:41]
	v_lshl_add_u64 v[50:51], v[0:1], 0, v[50:51]
	v_lshl_add_u64 v[40:41], v[0:1], 0, v[40:41]
	s_waitcnt lgkmcnt(0)
	global_store_dwordx4 v[50:51], v[56:59], off
	global_store_dwordx4 v[40:41], v[60:63], off
	s_add_i32 s18, s18, s21
	s_waitcnt vmcnt(8)
	s_cmp_lt_i32 s2, s13
	v_mov_b32_e32 v50, v27
	v_mov_b32_e32 v51, v92
	v_mov_b32_e32 v40, v93
	v_mov_b32_e32 v41, v94
	v_mov_b32_e32 v42, v95
	v_mov_b32_e32 v45, v96
	s_cbranch_scc0 .LBB8_8
